# final MoE combine token loop rewritten the same way (two tokens in flight, packed fp8 unpack); on top of attention + first combine rewrites
# baseline (speedup 1.0000x reference)
.LBB0_2049:
	s_or_b64 exec, exec, s[18:19]
	s_cmpk_gt_i32 s94, 0x7fff
	s_waitcnt lgkmcnt(0)
	s_barrier
	s_cbranch_scc1 .LBB0_2052
	s_load_dwordx2 s[2:3], s[0:1], 0xc8
	s_load_dwordx2 s[10:11], s[0:1], 0xc0
	v_lshlrev_b32_e32 v1, 4, v242
	v_add_u32_e32 v137, 0x1000, v1
	v_lshlrev_b32_e32 v2, 3, v242
	v_lshlrev_b32_e32 v136, 2, v242
	v_mov_b32_e32 v3, 0
	v_mov_b32_e32 v124, 0x20000
	v_mov_b32_e32 v125, 0x80000
	v_mov_b32_e32 v126, 0xa0000
	v_mov_b32_e32 v127, 0x24d00
	s_waitcnt lgkmcnt(0)
	s_add_u32 s4, s2, 0x19000000
	s_addc_u32 s5, s3, 0
	s_add_u32 s6, s2, 0x2e800000
	s_addc_u32 s7, s3, 0
	s_add_u32 s8, s2, 0x3600000
	s_addc_u32 s9, s3, 0
	s_mov_b32 s14, s94
	s_lshl_b32 s17, s14, 2
	s_add_u32 s30, s8, s17
	s_addc_u32 s31, s9, 0
	global_load_dword v4, v3, s[30:31]
	global_load_dword v5, v124, s[30:31]
	global_load_dword v6, v125, s[30:31]
	global_load_dword v7, v126, s[30:31]
	s_waitcnt vmcnt(0)
	v_lshrrev_b32_e32 v108, 24, v4
	v_lshrrev_b32_e32 v109, 24, v5
	v_lshl_add_u32 v108, v108, 2, v127
	v_lshl_add_u32 v109, v109, 2, v127
	ds_read_b32 v108, v108
	ds_read_b32 v109, v109
	v_and_b32_e32 v110, 0xffffff, v4
	v_and_b32_e32 v111, 0xffffff, v5
	v_mul_f32_e32 v128, 0x3d000000, v6
	v_mul_f32_e32 v130, 0x3d000000, v7
	v_mov_b32_e32 v129, v128
	v_mov_b32_e32 v131, v130
	s_lshr_b32 s18, s14, 20
	s_lshl_b32 s17, s14, 12
	s_add_u32 s24, s4, s17
	s_addc_u32 s25, s5, s18
	global_load_dwordx2 v[12:13], v2, s[24:25] offset:0
	global_load_dwordx2 v[14:15], v2, s[24:25] offset:512
	global_load_dwordx2 v[16:17], v2, s[24:25] offset:1024
	global_load_dwordx2 v[18:19], v2, s[24:25] offset:1536
	global_load_dwordx2 v[20:21], v2, s[24:25] offset:2048
	global_load_dwordx2 v[22:23], v2, s[24:25] offset:2560
	global_load_dwordx2 v[24:25], v2, s[24:25] offset:3072
	global_load_dwordx2 v[26:27], v2, s[24:25] offset:3584
	s_waitcnt lgkmcnt(0)
	v_add_u32_e32 v108, v108, v110
	v_add_u32_e32 v109, v109, v111
	s_nop 0
	v_readfirstlane_b32 s17, v108
	v_readfirstlane_b32 s18, v109
	s_nop 3
	s_lshr_b32 s31, s17, 21
	s_lshl_b32 s30, s17, 11
	s_add_u32 s26, s6, s30
	s_addc_u32 s27, s7, s31
	s_lshr_b32 s31, s18, 21
	s_lshl_b32 s30, s18, 11
	s_add_u32 s28, s6, s30
	s_addc_u32 s29, s7, s31
	global_load_dword v28, v136, s[26:27] offset:0
	global_load_dword v29, v136, s[26:27] offset:256
	global_load_dword v30, v136, s[26:27] offset:512
	global_load_dword v31, v136, s[26:27] offset:768
	global_load_dword v32, v136, s[26:27] offset:1024
	global_load_dword v33, v136, s[26:27] offset:1280
	global_load_dword v34, v136, s[26:27] offset:1536
	global_load_dword v35, v136, s[26:27] offset:1792
	global_load_dword v36, v136, s[28:29] offset:0
	global_load_dword v37, v136, s[28:29] offset:256
	global_load_dword v38, v136, s[28:29] offset:512
	global_load_dword v39, v136, s[28:29] offset:768
	global_load_dword v40, v136, s[28:29] offset:1024
	global_load_dword v41, v136, s[28:29] offset:1280
	global_load_dword v42, v136, s[28:29] offset:1536
	global_load_dword v43, v136, s[28:29] offset:1792
	s_add_i32 s15, s14, s92
	s_cmpk_lt_u32 s15, 0x8000
	s_cselect_b32 s15, s15, s14
	s_lshl_b32 s17, s15, 2
	s_add_u32 s30, s8, s17
	s_addc_u32 s31, s9, 0
	global_load_dword v8, v3, s[30:31]
	global_load_dword v9, v124, s[30:31]
	global_load_dword v10, v125, s[30:31]
	global_load_dword v11, v126, s[30:31]
	s_waitcnt vmcnt(0)
.Lcf_loop:
	s_waitcnt vmcnt(8)
	v_lshrrev_b32_e32 v108, 24, v8
	v_lshrrev_b32_e32 v109, 24, v9
	v_lshl_add_u32 v108, v108, 2, v127
	v_lshl_add_u32 v109, v109, 2, v127
	ds_read_b32 v108, v108
	ds_read_b32 v109, v109
	v_and_b32_e32 v110, 0xffffff, v8
	v_and_b32_e32 v111, 0xffffff, v9
	v_mul_f32_e32 v132, 0x3d000000, v10
	v_mul_f32_e32 v134, 0x3d000000, v11
	v_mov_b32_e32 v133, v132
	v_mov_b32_e32 v135, v134
	s_lshr_b32 s18, s15, 20
	s_lshl_b32 s17, s15, 12
	s_add_u32 s24, s4, s17
	s_addc_u32 s25, s5, s18
	global_load_dwordx2 v[44:45], v2, s[24:25] offset:0
	global_load_dwordx2 v[46:47], v2, s[24:25] offset:512
	global_load_dwordx2 v[48:49], v2, s[24:25] offset:1024
	global_load_dwordx2 v[50:51], v2, s[24:25] offset:1536
	global_load_dwordx2 v[52:53], v2, s[24:25] offset:2048
	global_load_dwordx2 v[54:55], v2, s[24:25] offset:2560
	global_load_dwordx2 v[56:57], v2, s[24:25] offset:3072
	global_load_dwordx2 v[58:59], v2, s[24:25] offset:3584
	s_waitcnt lgkmcnt(0)
	v_add_u32_e32 v108, v108, v110
	v_add_u32_e32 v109, v109, v111
	s_nop 0
	v_readfirstlane_b32 s17, v108
	v_readfirstlane_b32 s18, v109
	s_nop 3
	s_lshr_b32 s31, s17, 21
	s_lshl_b32 s30, s17, 11
	s_add_u32 s26, s6, s30
	s_addc_u32 s27, s7, s31
	s_lshr_b32 s31, s18, 21
	s_lshl_b32 s30, s18, 11
	s_add_u32 s28, s6, s30
	s_addc_u32 s29, s7, s31
	global_load_dword v60, v136, s[26:27] offset:0
	global_load_dword v61, v136, s[26:27] offset:256
	global_load_dword v62, v136, s[26:27] offset:512
	global_load_dword v63, v136, s[26:27] offset:768
	global_load_dword v64, v136, s[26:27] offset:1024
	global_load_dword v65, v136, s[26:27] offset:1280
	global_load_dword v66, v136, s[26:27] offset:1536
	global_load_dword v67, v136, s[26:27] offset:1792
	global_load_dword v68, v136, s[28:29] offset:0
	global_load_dword v69, v136, s[28:29] offset:256
	global_load_dword v70, v136, s[28:29] offset:512
	global_load_dword v71, v136, s[28:29] offset:768
	global_load_dword v72, v136, s[28:29] offset:1024
	global_load_dword v73, v136, s[28:29] offset:1280
	global_load_dword v74, v136, s[28:29] offset:1536
	global_load_dword v75, v136, s[28:29] offset:1792
	s_add_i32 s16, s15, s92
	s_cmpk_lt_u32 s16, 0x8000
	s_cselect_b32 s16, s16, s15
	s_lshl_b32 s17, s16, 2
	s_add_u32 s30, s8, s17
	s_addc_u32 s31, s9, 0
	global_load_dword v4, v3, s[30:31]
	global_load_dword v5, v124, s[30:31]
	global_load_dword v6, v125, s[30:31]
	global_load_dword v7, v126, s[30:31]
	s_lshr_b32 s18, s14, 19
	s_lshl_b32 s17, s14, 13
	s_add_u32 s34, s10, s17
	s_addc_u32 s35, s11, s18
	s_waitcnt vmcnt(40)
	v_lshlrev_b32_e32 v76, 16, v12
	v_and_b32_e32 v77, 0xffff0000, v12
	v_lshlrev_b32_e32 v78, 16, v13
	v_and_b32_e32 v79, 0xffff0000, v13
	v_lshlrev_b32_e32 v80, 16, v14
	v_and_b32_e32 v81, 0xffff0000, v14
	v_lshlrev_b32_e32 v82, 16, v15
	v_and_b32_e32 v83, 0xffff0000, v15
	v_lshlrev_b32_e32 v84, 16, v16
	v_and_b32_e32 v85, 0xffff0000, v16
	v_lshlrev_b32_e32 v86, 16, v17
	v_and_b32_e32 v87, 0xffff0000, v17
	v_lshlrev_b32_e32 v88, 16, v18
	v_and_b32_e32 v89, 0xffff0000, v18
	v_lshlrev_b32_e32 v90, 16, v19
	v_and_b32_e32 v91, 0xffff0000, v19
	v_lshlrev_b32_e32 v92, 16, v20
	v_and_b32_e32 v93, 0xffff0000, v20
	v_lshlrev_b32_e32 v94, 16, v21
	v_and_b32_e32 v95, 0xffff0000, v21
	v_lshlrev_b32_e32 v96, 16, v22
	v_and_b32_e32 v97, 0xffff0000, v22
	v_lshlrev_b32_e32 v98, 16, v23
	v_and_b32_e32 v99, 0xffff0000, v23
	v_lshlrev_b32_e32 v100, 16, v24
	v_and_b32_e32 v101, 0xffff0000, v24
	v_lshlrev_b32_e32 v102, 16, v25
	v_and_b32_e32 v103, 0xffff0000, v25
	v_lshlrev_b32_e32 v104, 16, v26
	v_and_b32_e32 v105, 0xffff0000, v26
	v_lshlrev_b32_e32 v106, 16, v27
	v_and_b32_e32 v107, 0xffff0000, v27
	v_cvt_pk_f32_fp8_e32 v[108:109], v28
	v_cvt_pk_f32_fp8_sdwa v[110:111], v28 src0_sel:WORD_1
	v_pk_fma_f32 v[76:77], v[108:109], v[128:129], v[76:77]
	v_pk_fma_f32 v[78:79], v[110:111], v[128:129], v[78:79]
	v_cvt_pk_f32_fp8_e32 v[108:109], v29
	v_cvt_pk_f32_fp8_sdwa v[110:111], v29 src0_sel:WORD_1
	v_pk_fma_f32 v[80:81], v[108:109], v[128:129], v[80:81]
	v_pk_fma_f32 v[82:83], v[110:111], v[128:129], v[82:83]
	v_cvt_pk_f32_fp8_e32 v[108:109], v30
	v_cvt_pk_f32_fp8_sdwa v[110:111], v30 src0_sel:WORD_1
	v_pk_fma_f32 v[84:85], v[108:109], v[128:129], v[84:85]
	v_pk_fma_f32 v[86:87], v[110:111], v[128:129], v[86:87]
	v_cvt_pk_f32_fp8_e32 v[108:109], v31
	v_cvt_pk_f32_fp8_sdwa v[110:111], v31 src0_sel:WORD_1
	v_pk_fma_f32 v[88:89], v[108:109], v[128:129], v[88:89]
	v_pk_fma_f32 v[90:91], v[110:111], v[128:129], v[90:91]
	v_cvt_pk_f32_fp8_e32 v[108:109], v32
	v_cvt_pk_f32_fp8_sdwa v[110:111], v32 src0_sel:WORD_1
	v_pk_fma_f32 v[92:93], v[108:109], v[128:129], v[92:93]
	v_pk_fma_f32 v[94:95], v[110:111], v[128:129], v[94:95]
	v_cvt_pk_f32_fp8_e32 v[108:109], v33
	v_cvt_pk_f32_fp8_sdwa v[110:111], v33 src0_sel:WORD_1
	v_pk_fma_f32 v[96:97], v[108:109], v[128:129], v[96:97]
	v_pk_fma_f32 v[98:99], v[110:111], v[128:129], v[98:99]
	v_cvt_pk_f32_fp8_e32 v[108:109], v34
	v_cvt_pk_f32_fp8_sdwa v[110:111], v34 src0_sel:WORD_1
	v_pk_fma_f32 v[100:101], v[108:109], v[128:129], v[100:101]
	v_pk_fma_f32 v[102:103], v[110:111], v[128:129], v[102:103]
	v_cvt_pk_f32_fp8_e32 v[108:109], v35
	v_cvt_pk_f32_fp8_sdwa v[110:111], v35 src0_sel:WORD_1
	v_pk_fma_f32 v[104:105], v[108:109], v[128:129], v[104:105]
	v_pk_fma_f32 v[106:107], v[110:111], v[128:129], v[106:107]
	v_cvt_pk_f32_fp8_e32 v[108:109], v36
	v_cvt_pk_f32_fp8_sdwa v[110:111], v36 src0_sel:WORD_1
	v_pk_fma_f32 v[76:77], v[108:109], v[130:131], v[76:77]
	v_pk_fma_f32 v[78:79], v[110:111], v[130:131], v[78:79]
	v_cvt_pk_f32_fp8_e32 v[108:109], v37
	v_cvt_pk_f32_fp8_sdwa v[110:111], v37 src0_sel:WORD_1
	v_pk_fma_f32 v[80:81], v[108:109], v[130:131], v[80:81]
	v_pk_fma_f32 v[82:83], v[110:111], v[130:131], v[82:83]
	v_cvt_pk_f32_fp8_e32 v[108:109], v38
	v_cvt_pk_f32_fp8_sdwa v[110:111], v38 src0_sel:WORD_1
	v_pk_fma_f32 v[84:85], v[108:109], v[130:131], v[84:85]
	v_pk_fma_f32 v[86:87], v[110:111], v[130:131], v[86:87]
	v_cvt_pk_f32_fp8_e32 v[108:109], v39
	v_cvt_pk_f32_fp8_sdwa v[110:111], v39 src0_sel:WORD_1
	v_pk_fma_f32 v[88:89], v[108:109], v[130:131], v[88:89]
	v_pk_fma_f32 v[90:91], v[110:111], v[130:131], v[90:91]
	v_cvt_pk_f32_fp8_e32 v[108:109], v40
	v_cvt_pk_f32_fp8_sdwa v[110:111], v40 src0_sel:WORD_1
	v_pk_fma_f32 v[92:93], v[108:109], v[130:131], v[92:93]
	v_pk_fma_f32 v[94:95], v[110:111], v[130:131], v[94:95]
	v_cvt_pk_f32_fp8_e32 v[108:109], v41
	v_cvt_pk_f32_fp8_sdwa v[110:111], v41 src0_sel:WORD_1
	v_pk_fma_f32 v[96:97], v[108:109], v[130:131], v[96:97]
	v_pk_fma_f32 v[98:99], v[110:111], v[130:131], v[98:99]
	v_cvt_pk_f32_fp8_e32 v[108:109], v42
	v_cvt_pk_f32_fp8_sdwa v[110:111], v42 src0_sel:WORD_1
	v_pk_fma_f32 v[100:101], v[108:109], v[130:131], v[100:101]
	v_pk_fma_f32 v[102:103], v[110:111], v[130:131], v[102:103]
	v_cvt_pk_f32_fp8_e32 v[108:109], v43
	v_cvt_pk_f32_fp8_sdwa v[110:111], v43 src0_sel:WORD_1
	v_pk_fma_f32 v[104:105], v[108:109], v[130:131], v[104:105]
	v_pk_fma_f32 v[106:107], v[110:111], v[130:131], v[106:107]
	global_store_dwordx4 v1, v[76:79], s[34:35] offset:0
	global_store_dwordx4 v1, v[80:83], s[34:35] offset:1024
	global_store_dwordx4 v1, v[84:87], s[34:35] offset:2048
	global_store_dwordx4 v1, v[88:91], s[34:35] offset:3072
	global_store_dwordx4 v137, v[92:95], s[34:35] offset:0
	global_store_dwordx4 v137, v[96:99], s[34:35] offset:1024
	global_store_dwordx4 v137, v[100:103], s[34:35] offset:2048
	global_store_dwordx4 v137, v[104:107], s[34:35] offset:3072
	s_add_i32 s14, s14, s92
	s_mov_b32 s15, s16
	s_cmpk_lt_u32 s14, 0x8000
	s_cbranch_scc0 .Lcf_done
	s_waitcnt vmcnt(8)
	v_lshrrev_b32_e32 v108, 24, v4
	v_lshrrev_b32_e32 v109, 24, v5
	v_lshl_add_u32 v108, v108, 2, v127
	v_lshl_add_u32 v109, v109, 2, v127
	ds_read_b32 v108, v108
	ds_read_b32 v109, v109
	v_and_b32_e32 v110, 0xffffff, v4
	v_and_b32_e32 v111, 0xffffff, v5
	v_mul_f32_e32 v128, 0x3d000000, v6
	v_mul_f32_e32 v130, 0x3d000000, v7
	v_mov_b32_e32 v129, v128
	v_mov_b32_e32 v131, v130
	s_lshr_b32 s18, s15, 20
	s_lshl_b32 s17, s15, 12
	s_add_u32 s24, s4, s17
	s_addc_u32 s25, s5, s18
	global_load_dwordx2 v[12:13], v2, s[24:25] offset:0
	global_load_dwordx2 v[14:15], v2, s[24:25] offset:512
	global_load_dwordx2 v[16:17], v2, s[24:25] offset:1024
	global_load_dwordx2 v[18:19], v2, s[24:25] offset:1536
	global_load_dwordx2 v[20:21], v2, s[24:25] offset:2048
	global_load_dwordx2 v[22:23], v2, s[24:25] offset:2560
	global_load_dwordx2 v[24:25], v2, s[24:25] offset:3072
	global_load_dwordx2 v[26:27], v2, s[24:25] offset:3584
	s_waitcnt lgkmcnt(0)
	v_add_u32_e32 v108, v108, v110
	v_add_u32_e32 v109, v109, v111
	s_nop 0
	v_readfirstlane_b32 s17, v108
	v_readfirstlane_b32 s18, v109
	s_nop 3
	s_lshr_b32 s31, s17, 21
	s_lshl_b32 s30, s17, 11
	s_add_u32 s26, s6, s30
	s_addc_u32 s27, s7, s31
	s_lshr_b32 s31, s18, 21
	s_lshl_b32 s30, s18, 11
	s_add_u32 s28, s6, s30
	s_addc_u32 s29, s7, s31
	global_load_dword v28, v136, s[26:27] offset:0
	global_load_dword v29, v136, s[26:27] offset:256
	global_load_dword v30, v136, s[26:27] offset:512
	global_load_dword v31, v136, s[26:27] offset:768
	global_load_dword v32, v136, s[26:27] offset:1024
	global_load_dword v33, v136, s[26:27] offset:1280
	global_load_dword v34, v136, s[26:27] offset:1536
	global_load_dword v35, v136, s[26:27] offset:1792
	global_load_dword v36, v136, s[28:29] offset:0
	global_load_dword v37, v136, s[28:29] offset:256
	global_load_dword v38, v136, s[28:29] offset:512
	global_load_dword v39, v136, s[28:29] offset:768
	global_load_dword v40, v136, s[28:29] offset:1024
	global_load_dword v41, v136, s[28:29] offset:1280
	global_load_dword v42, v136, s[28:29] offset:1536
	global_load_dword v43, v136, s[28:29] offset:1792
	s_add_i32 s16, s15, s92
	s_cmpk_lt_u32 s16, 0x8000
	s_cselect_b32 s16, s16, s15
	s_lshl_b32 s17, s16, 2
	s_add_u32 s30, s8, s17
	s_addc_u32 s31, s9, 0
	global_load_dword v8, v3, s[30:31]
	global_load_dword v9, v124, s[30:31]
	global_load_dword v10, v125, s[30:31]
	global_load_dword v11, v126, s[30:31]
	s_lshr_b32 s18, s14, 19
	s_lshl_b32 s17, s14, 13
	s_add_u32 s34, s10, s17
	s_addc_u32 s35, s11, s18
	s_waitcnt vmcnt(40)
	v_lshlrev_b32_e32 v76, 16, v44
	v_and_b32_e32 v77, 0xffff0000, v44
	v_lshlrev_b32_e32 v78, 16, v45
	v_and_b32_e32 v79, 0xffff0000, v45
	v_lshlrev_b32_e32 v80, 16, v46
	v_and_b32_e32 v81, 0xffff0000, v46
	v_lshlrev_b32_e32 v82, 16, v47
	v_and_b32_e32 v83, 0xffff0000, v47
	v_lshlrev_b32_e32 v84, 16, v48
	v_and_b32_e32 v85, 0xffff0000, v48
	v_lshlrev_b32_e32 v86, 16, v49
	v_and_b32_e32 v87, 0xffff0000, v49
	v_lshlrev_b32_e32 v88, 16, v50
	v_and_b32_e32 v89, 0xffff0000, v50
	v_lshlrev_b32_e32 v90, 16, v51
	v_and_b32_e32 v91, 0xffff0000, v51
	v_lshlrev_b32_e32 v92, 16, v52
	v_and_b32_e32 v93, 0xffff0000, v52
	v_lshlrev_b32_e32 v94, 16, v53
	v_and_b32_e32 v95, 0xffff0000, v53
	v_lshlrev_b32_e32 v96, 16, v54
	v_and_b32_e32 v97, 0xffff0000, v54
	v_lshlrev_b32_e32 v98, 16, v55
	v_and_b32_e32 v99, 0xffff0000, v55
	v_lshlrev_b32_e32 v100, 16, v56
	v_and_b32_e32 v101, 0xffff0000, v56
	v_lshlrev_b32_e32 v102, 16, v57
	v_and_b32_e32 v103, 0xffff0000, v57
	v_lshlrev_b32_e32 v104, 16, v58
	v_and_b32_e32 v105, 0xffff0000, v58
	v_lshlrev_b32_e32 v106, 16, v59
	v_and_b32_e32 v107, 0xffff0000, v59
	v_cvt_pk_f32_fp8_e32 v[108:109], v60
	v_cvt_pk_f32_fp8_sdwa v[110:111], v60 src0_sel:WORD_1
	v_pk_fma_f32 v[76:77], v[108:109], v[132:133], v[76:77]
	v_pk_fma_f32 v[78:79], v[110:111], v[132:133], v[78:79]
	v_cvt_pk_f32_fp8_e32 v[108:109], v61
	v_cvt_pk_f32_fp8_sdwa v[110:111], v61 src0_sel:WORD_1
	v_pk_fma_f32 v[80:81], v[108:109], v[132:133], v[80:81]
	v_pk_fma_f32 v[82:83], v[110:111], v[132:133], v[82:83]
	v_cvt_pk_f32_fp8_e32 v[108:109], v62
	v_cvt_pk_f32_fp8_sdwa v[110:111], v62 src0_sel:WORD_1
	v_pk_fma_f32 v[84:85], v[108:109], v[132:133], v[84:85]
	v_pk_fma_f32 v[86:87], v[110:111], v[132:133], v[86:87]
	v_cvt_pk_f32_fp8_e32 v[108:109], v63
	v_cvt_pk_f32_fp8_sdwa v[110:111], v63 src0_sel:WORD_1
	v_pk_fma_f32 v[88:89], v[108:109], v[132:133], v[88:89]
	v_pk_fma_f32 v[90:91], v[110:111], v[132:133], v[90:91]
	v_cvt_pk_f32_fp8_e32 v[108:109], v64
	v_cvt_pk_f32_fp8_sdwa v[110:111], v64 src0_sel:WORD_1
	v_pk_fma_f32 v[92:93], v[108:109], v[132:133], v[92:93]
	v_pk_fma_f32 v[94:95], v[110:111], v[132:133], v[94:95]
	v_cvt_pk_f32_fp8_e32 v[108:109], v65
	v_cvt_pk_f32_fp8_sdwa v[110:111], v65 src0_sel:WORD_1
	v_pk_fma_f32 v[96:97], v[108:109], v[132:133], v[96:97]
	v_pk_fma_f32 v[98:99], v[110:111], v[132:133], v[98:99]
	v_cvt_pk_f32_fp8_e32 v[108:109], v66
	v_cvt_pk_f32_fp8_sdwa v[110:111], v66 src0_sel:WORD_1
	v_pk_fma_f32 v[100:101], v[108:109], v[132:133], v[100:101]
	v_pk_fma_f32 v[102:103], v[110:111], v[132:133], v[102:103]
	v_cvt_pk_f32_fp8_e32 v[108:109], v67
	v_cvt_pk_f32_fp8_sdwa v[110:111], v67 src0_sel:WORD_1
	v_pk_fma_f32 v[104:105], v[108:109], v[132:133], v[104:105]
	v_pk_fma_f32 v[106:107], v[110:111], v[132:133], v[106:107]
	v_cvt_pk_f32_fp8_e32 v[108:109], v68
	v_cvt_pk_f32_fp8_sdwa v[110:111], v68 src0_sel:WORD_1
	v_pk_fma_f32 v[76:77], v[108:109], v[134:135], v[76:77]
	v_pk_fma_f32 v[78:79], v[110:111], v[134:135], v[78:79]
	v_cvt_pk_f32_fp8_e32 v[108:109], v69
	v_cvt_pk_f32_fp8_sdwa v[110:111], v69 src0_sel:WORD_1
	v_pk_fma_f32 v[80:81], v[108:109], v[134:135], v[80:81]
	v_pk_fma_f32 v[82:83], v[110:111], v[134:135], v[82:83]
	v_cvt_pk_f32_fp8_e32 v[108:109], v70
	v_cvt_pk_f32_fp8_sdwa v[110:111], v70 src0_sel:WORD_1
	v_pk_fma_f32 v[84:85], v[108:109], v[134:135], v[84:85]
	v_pk_fma_f32 v[86:87], v[110:111], v[134:135], v[86:87]
	v_cvt_pk_f32_fp8_e32 v[108:109], v71
	v_cvt_pk_f32_fp8_sdwa v[110:111], v71 src0_sel:WORD_1
	v_pk_fma_f32 v[88:89], v[108:109], v[134:135], v[88:89]
	v_pk_fma_f32 v[90:91], v[110:111], v[134:135], v[90:91]
	v_cvt_pk_f32_fp8_e32 v[108:109], v72
	v_cvt_pk_f32_fp8_sdwa v[110:111], v72 src0_sel:WORD_1
	v_pk_fma_f32 v[92:93], v[108:109], v[134:135], v[92:93]
	v_pk_fma_f32 v[94:95], v[110:111], v[134:135], v[94:95]
	v_cvt_pk_f32_fp8_e32 v[108:109], v73
	v_cvt_pk_f32_fp8_sdwa v[110:111], v73 src0_sel:WORD_1
	v_pk_fma_f32 v[96:97], v[108:109], v[134:135], v[96:97]
	v_pk_fma_f32 v[98:99], v[110:111], v[134:135], v[98:99]
	v_cvt_pk_f32_fp8_e32 v[108:109], v74
	v_cvt_pk_f32_fp8_sdwa v[110:111], v74 src0_sel:WORD_1
	v_pk_fma_f32 v[100:101], v[108:109], v[134:135], v[100:101]
	v_pk_fma_f32 v[102:103], v[110:111], v[134:135], v[102:103]
	v_cvt_pk_f32_fp8_e32 v[108:109], v75
	v_cvt_pk_f32_fp8_sdwa v[110:111], v75 src0_sel:WORD_1
	v_pk_fma_f32 v[104:105], v[108:109], v[134:135], v[104:105]
	v_pk_fma_f32 v[106:107], v[110:111], v[134:135], v[106:107]
	global_store_dwordx4 v1, v[76:79], s[34:35] offset:0
	global_store_dwordx4 v1, v[80:83], s[34:35] offset:1024
	global_store_dwordx4 v1, v[84:87], s[34:35] offset:2048
	global_store_dwordx4 v1, v[88:91], s[34:35] offset:3072
	global_store_dwordx4 v137, v[92:95], s[34:35] offset:0
	global_store_dwordx4 v137, v[96:99], s[34:35] offset:1024
	global_store_dwordx4 v137, v[100:103], s[34:35] offset:2048
	global_store_dwordx4 v137, v[104:107], s[34:35] offset:3072
	s_add_i32 s14, s14, s92
	s_mov_b32 s15, s16
	s_cmpk_lt_u32 s14, 0x8000
	s_cbranch_scc1 .Lcf_loop
.Lcf_done:
.LBB0_2052:
	s_endpgm
